# baseline (speedup 1.0000x reference)
.LBB1_13:
	v_mfma_f32_32x32x16_bf16 v[2:17], v[78:81], v[206:209], v[236:251]
	ds_read_b128 v[174:177], v210
	v_add_u32_e32 v195, v230, v228
	v_mfma_f32_32x32x16_bf16 v[2:17], v[74:77], v[190:193], v[2:17]
	ds_read_b128 v[170:173], v210 offset:1024
	v_exp_f32_e32 v199, v28
	v_exp_f32_e32 v198, v32
	v_mfma_f32_32x32x16_bf16 v[2:17], v[70:73], v[158:161], v[2:17]
	ds_read_b128 v[166:169], v210 offset:2048
	v_exp_f32_e32 v197, v20
	v_exp_f32_e32 v196, v24
	v_exp_f32_e32 v18, v18
	v_exp_f32_e32 v22, v22
	v_exp_f32_e32 v24, v26
	v_exp_f32_e32 v26, v30
	v_fma_f32 v20, v197, s12, s12
	v_fma_f32 v28, v196, s12, s12
	v_fma_f32 v30, v199, s12, s12
	v_fma_f32 v32, v198, s12, s12
	v_mfma_f32_32x32x16_bf16 v[2:17], v[66:69], v[142:145], v[2:17]
	ds_read_b128 v[162:165], v210 offset:3072
	v_exp_f32_e32 v19, v19
	v_exp_f32_e32 v23, v23
	v_exp_f32_e32 v27, v27
	v_exp_f32_e32 v31, v31
	v_fmac_f32_e32 v20, v18, v20
	v_fmac_f32_e32 v28, v22, v28
	v_fmac_f32_e32 v30, v24, v30
	v_fmac_f32_e32 v32, v26, v32
	v_mfma_f32_32x32x16_bf16 v[2:17], v[62:65], v[154:157], v[2:17]
	ds_read_b128 v[158:161], v210 offset:4096
	v_add_f32_e32 v22, 1.0, v19
	v_rcp_f32_e32 v19, v20
	v_rcp_f32_e32 v18, v28
	v_add_f32_e32 v20, 1.0, v23
	v_rcp_f32_e32 v191, v30
	v_rcp_f32_e32 v190, v32
	v_mfma_f32_32x32x16_bf16 v[2:17], v[58:61], v[182:185], v[2:17]
	ds_read_b128 v[154:157], v210 offset:5120
	v_exp_f32_e32 v206, v21
	v_exp_f32_e32 v207, v25
	v_add_f32_e32 v23, 1.0, v27
	v_rcp_f32_e32 v192, v20
	v_add_f32_e32 v20, 1.0, v31
	v_rcp_f32_e32 v193, v22
	v_mfma_f32_32x32x16_bf16 v[2:17], v[54:57], v[186:189], v[2:17]
	ds_read_b128 v[142:145], v210 offset:6144
	v_exp_f32_e32 v208, v29
	v_exp_f32_e32 v209, v33
	v_rcp_f32_e32 v183, v23
	v_rcp_f32_e32 v182, v20
	v_mfma_f32_32x32x16_bf16 v[2:17], v[50:53], v[134:137], v[2:17]
	ds_read_b128 v[130:133], v210 offset:7168
	v_fma_f32 v186, -v196, v18, v18
	v_fma_f32 v187, -v197, v19, v19
	ds_read_b128 v[18:21], v231 offset:36928
	ds_read_b128 v[22:25], v231 offset:36944
	ds_read_b128 v[26:29], v231 offset:36960
	ds_read_b128 v[30:33], v231 offset:36976
	v_pk_fma_f32 v[200:201], v[192:193], v[220:221], v[186:187]
	v_pk_fma_f32 v[134:135], v[198:199], v[190:191], v[190:191] neg_lo:[1,0,0] neg_hi:[1,0,0]
	s_nop 0
	v_pk_fma_f32 v[198:199], v[182:183], v[222:223], v[134:135]
	v_mfma_f32_32x32x16_bf16 v[2:17], v[46:49], v[138:141], v[2:17]
	ds_read_b128 v[134:137], v195 offset:16384
	v_add_f32_e32 v182, 1.0, v206
	v_exp_f32_e32 v183, v201
	v_exp_f32_e32 v186, v200
	v_exp_f32_e32 v187, v199
	v_exp_f32_e32 v188, v198
	v_add_f32_e32 v189, 1.0, v207
	v_add_f32_e32 v190, 1.0, v208
	v_add_f32_e32 v191, 1.0, v209
	v_mfma_f32_32x32x16_bf16 v[2:17], v[42:45], v[146:149], v[2:17]
	ds_read_b128 v[138:141], v195 offset:16416
	v_fmac_f32_e32 v182, v182, v183
	v_fmac_f32_e32 v189, v189, v186
	v_fmac_f32_e32 v190, v190, v187
	v_fmac_f32_e32 v191, v191, v188
	v_mfma_f32_32x32x16_bf16 v[2:17], v[38:41], v[150:153], v[2:17]
	ds_read_b128 v[146:149], v195 offset:16448
	v_rcp_f32_e32 v182, v182
	v_rcp_f32_e32 v189, v189
	v_mfma_f32_32x32x16_bf16 v[2:17], v[34:37], v[178:181], v[2:17]
	ds_read_b128 v[150:153], v195 offset:16480
	v_rcp_f32_e32 v190, v190
	v_rcp_f32_e32 v191, v191
	v_fma_f32 v182, -v183, v182, v182
	v_fma_f32 v183, -v186, v189, v189
	s_waitcnt lgkmcnt(4)
	v_mfma_f32_32x32x16_bf16 v[18:33], v[126:129], v[174:177], v[18:33]
	v_fma_f32 v186, -v187, v190, v190
	v_fma_f32 v187, -v188, v191, v191
	v_cvt_pk_bf16_f32 v252, v182, v183
	v_cvt_pk_bf16_f32 v253, v186, v187
	v_mfma_f32_32x32x16_bf16 v[18:33], v[122:125], v[170:173], v[18:33]
	s_nop 1
	v_exp_f32_e32 v179, v4
	v_exp_f32_e32 v178, v8
	v_exp_f32_e32 v181, v12
	v_exp_f32_e32 v180, v16
	v_mfma_f32_32x32x16_bf16 v[18:33], v[118:121], v[166:169], v[18:33]
	v_exp_f32_e32 v2, v2
	v_exp_f32_e32 v6, v6
	v_exp_f32_e32 v10, v10
	v_exp_f32_e32 v12, v14
	v_fma_f32 v4, v179, s12, s12
	v_fma_f32 v8, v178, s12, s12
	v_fma_f32 v14, v181, s12, s12
	v_fma_f32 v16, v180, s12, s12
	v_mfma_f32_32x32x16_bf16 v[18:33], v[114:117], v[162:165], v[18:33]
	v_exp_f32_e32 v3, v3
	v_fmac_f32_e32 v4, v2, v4
	v_exp_f32_e32 v2, v7
	v_fmac_f32_e32 v8, v6, v8
	v_exp_f32_e32 v6, v11
	v_exp_f32_e32 v7, v15
	v_fmac_f32_e32 v14, v10, v14
	v_fmac_f32_e32 v16, v12, v16
	v_mfma_f32_32x32x16_bf16 v[18:33], v[110:113], v[158:161], v[18:33]
	v_add_f32_e32 v10, 1.0, v3
	v_rcp_f32_e32 v3, v4
	v_add_f32_e32 v4, 1.0, v2
	v_rcp_f32_e32 v2, v8
	v_rcp_f32_e32 v183, v14
	v_rcp_f32_e32 v182, v16
	v_mfma_f32_32x32x16_bf16 v[18:33], v[106:109], v[154:157], v[18:33]
	v_add_f32_e32 v6, 1.0, v6
	v_add_f32_e32 v7, 1.0, v7
	v_rcp_f32_e32 v187, v10
	v_rcp_f32_e32 v186, v4
	v_exp_f32_e32 v190, v5
	v_exp_f32_e32 v191, v9
	v_mfma_f32_32x32x16_bf16 v[18:33], v[102:105], v[142:145], v[18:33]
	v_rcp_f32_e32 v189, v6
	v_rcp_f32_e32 v188, v7
	v_exp_f32_e32 v192, v13
	v_exp_f32_e32 v193, v17
	v_mfma_f32_32x32x16_bf16 v[18:33], v[98:101], v[130:133], v[18:33]
	v_fma_f32 v178, -v178, v2, v2
	v_fma_f32 v179, -v179, v3, v3
	v_pk_fma_f32 v[206:207], v[186:187], v[216:217], v[178:179]
	s_nop 0
	v_pk_fma_f32 v[178:179], v[180:181], v[182:183], v[182:183] neg_lo:[1,0,0] neg_hi:[1,0,0]
	s_nop 0
	v_pk_fma_f32 v[208:209], v[188:189], v[218:219], v[178:179]
	s_waitcnt lgkmcnt(0)
	v_mfma_f32_32x32x16_bf16 v[18:33], v[94:97], v[134:137], v[18:33]
	v_add_f32_e32 v178, 1.0, v190
	v_exp_f32_e32 v179, v207
	v_add_f32_e32 v180, 1.0, v191
	v_exp_f32_e32 v181, v206
	v_exp_f32_e32 v182, v209
	v_exp_f32_e32 v183, v208
	v_add_f32_e32 v184, 1.0, v192
	v_add_f32_e32 v185, 1.0, v193
	v_mfma_f32_32x32x16_bf16 v[18:33], v[90:93], v[138:141], v[18:33]
	v_fmac_f32_e32 v178, v178, v179
	v_fmac_f32_e32 v180, v180, v181
	v_fmac_f32_e32 v184, v184, v182
	v_fmac_f32_e32 v185, v185, v183
	v_mfma_f32_32x32x16_bf16 v[18:33], v[86:89], v[146:149], v[18:33]
	v_rcp_f32_e32 v178, v178
	v_rcp_f32_e32 v180, v180
	v_rcp_f32_e32 v184, v184
	v_rcp_f32_e32 v185, v185
	v_mfma_f32_32x32x16_bf16 v[18:33], v[82:85], v[150:153], v[18:33]
	v_fma_f32 v178, -v179, v178, v178
	v_fma_f32 v179, -v181, v180, v180
	v_fma_f32 v180, -v182, v184, v184
	v_fma_f32 v181, -v183, v185, v185
	v_cvt_pk_bf16_f32 v254, v178, v179
	v_cvt_pk_bf16_f32 v255, v180, v181
	ds_write_b128 v211, v[252:255] offset:8192
	s_waitcnt lgkmcnt(0)
	s_barrier
	s_add_i32 s1, s1, 2
	s_cmp_gt_u32 s1, 16
	v_add_u32_e32 v232, 0x200, v232
	s_cbranch_scc1 .LBB1_30
.LBB1_14:
	v_mfma_f32_32x32x16_bf16 v[2:17], v[78:81], v[174:177], v[236:251]
	v_add_u32_e32 v192, v230, v229
	ds_read2_b32 v[228:229], v232 offset1:32
	ds_read_b128 v[194:197], v210 offset:8192
	v_mfma_f32_32x32x16_bf16 v[2:17], v[74:77], v[170:173], v[2:17]
	ds_read_b128 v[178:181], v210 offset:9216
	v_exp_f32_e32 v187, v20
	v_exp_f32_e32 v186, v24
	v_mfma_f32_32x32x16_bf16 v[2:17], v[70:73], v[166:169], v[2:17]
	ds_read_b128 v[170:173], v210 offset:10240
	v_exp_f32_e32 v189, v28
	v_exp_f32_e32 v188, v32
	v_exp_f32_e32 v18, v18
	v_exp_f32_e32 v22, v22
	v_exp_f32_e32 v24, v26
	v_exp_f32_e32 v26, v30
	v_fma_f32 v20, v187, s12, s12
	v_fma_f32 v28, v186, s12, s12
	v_fma_f32 v30, v189, s12, s12
	v_fma_f32 v32, v188, s12, s12
	v_mfma_f32_32x32x16_bf16 v[2:17], v[66:69], v[162:165], v[2:17]
	ds_read_b128 v[166:169], v210 offset:11264
	v_exp_f32_e32 v19, v19
	v_exp_f32_e32 v23, v23
	v_exp_f32_e32 v27, v27
	v_exp_f32_e32 v31, v31
	v_fmac_f32_e32 v20, v18, v20
	v_fmac_f32_e32 v28, v22, v28
	v_fmac_f32_e32 v30, v24, v30
	v_fmac_f32_e32 v32, v26, v32
	v_mfma_f32_32x32x16_bf16 v[2:17], v[62:65], v[158:161], v[2:17]
	ds_read_b128 v[162:165], v210 offset:12288
	v_add_f32_e32 v22, 1.0, v19
	v_rcp_f32_e32 v19, v20
	v_rcp_f32_e32 v18, v28
	v_rcp_f32_e32 v191, v30
	v_rcp_f32_e32 v190, v32
	v_add_f32_e32 v20, 1.0, v23
	v_mfma_f32_32x32x16_bf16 v[2:17], v[58:61], v[154:157], v[2:17]
	ds_read_b128 v[174:177], v210 offset:13312
	v_rcp_f32_e32 v159, v22
	v_rcp_f32_e32 v158, v20
	v_exp_f32_e32 v160, v21
	v_exp_f32_e32 v161, v25
	v_add_f32_e32 v23, 1.0, v27
	v_add_f32_e32 v20, 1.0, v31
	v_mfma_f32_32x32x16_bf16 v[2:17], v[54:57], v[142:145], v[2:17]
	ds_read_b128 v[182:185], v210 offset:14336
	v_rcp_f32_e32 v155, v23
	v_rcp_f32_e32 v154, v20
	v_exp_f32_e32 v193, v29
	v_exp_f32_e32 v217, v33
	v_mfma_f32_32x32x16_bf16 v[2:17], v[50:53], v[130:133], v[2:17]
	ds_read_b128 v[142:145], v210 offset:15360
	v_fma_f32 v156, -v186, v18, v18
	v_fma_f32 v157, -v187, v19, v19
	ds_read_b128 v[18:21], v231 offset:36928
	ds_read_b128 v[22:25], v231 offset:36944
	ds_read_b128 v[26:29], v231 offset:36960
	ds_read_b128 v[30:33], v231 offset:36976
	v_pk_fma_f32 v[214:215], v[158:159], v[214:215], v[156:157]
	v_pk_fma_f32 v[130:131], v[188:189], v[190:191], v[190:191] neg_lo:[1,0,0] neg_hi:[1,0,0]
	s_nop 0
	v_pk_fma_f32 v[212:213], v[154:155], v[212:213], v[130:131]
	v_mfma_f32_32x32x16_bf16 v[2:17], v[46:49], v[134:137], v[2:17]
	ds_read_b128 v[154:157], v192 offset:16384
	v_add_f32_e32 v130, 1.0, v160
	v_exp_f32_e32 v131, v215
	v_exp_f32_e32 v132, v214
	v_exp_f32_e32 v133, v213
	v_exp_f32_e32 v220, v212
	v_add_f32_e32 v134, 1.0, v161
	v_add_f32_e32 v135, 1.0, v193
	v_add_f32_e32 v136, 1.0, v217
	v_mfma_f32_32x32x16_bf16 v[2:17], v[42:45], v[138:141], v[2:17]
	ds_read_b128 v[158:161], v192 offset:16416
	v_fmac_f32_e32 v130, v130, v131
	v_fmac_f32_e32 v134, v134, v132
	v_fmac_f32_e32 v135, v135, v133
	v_fmac_f32_e32 v136, v136, v220
	v_mfma_f32_32x32x16_bf16 v[2:17], v[38:41], v[146:149], v[2:17]
	ds_read_b128 v[186:189], v192 offset:16448
	v_rcp_f32_e32 v130, v130
	v_rcp_f32_e32 v134, v134
	v_mfma_f32_32x32x16_bf16 v[2:17], v[34:37], v[150:153], v[2:17]
	ds_read_b128 v[190:193], v192 offset:16480
	v_rcp_f32_e32 v135, v135
	v_rcp_f32_e32 v136, v136
	v_fma_f32 v130, -v131, v130, v130
	v_fma_f32 v131, -v132, v134, v134
	s_waitcnt lgkmcnt(4)
	v_mfma_f32_32x32x16_bf16 v[18:33], v[126:129], v[194:197], v[18:33]
	v_fma_f32 v132, -v133, v135, v135
	v_fma_f32 v133, -v220, v136, v136
	v_cvt_pk_bf16_f32 v252, v130, v131
	v_cvt_pk_bf16_f32 v253, v132, v133
	v_mfma_f32_32x32x16_bf16 v[18:33], v[122:125], v[178:181], v[18:33]
	s_nop 1
	v_exp_f32_e32 v131, v4
	v_exp_f32_e32 v130, v8
	v_exp_f32_e32 v133, v12
	v_exp_f32_e32 v132, v16
	v_mfma_f32_32x32x16_bf16 v[18:33], v[118:121], v[170:173], v[18:33]
	v_exp_f32_e32 v2, v2
	v_exp_f32_e32 v6, v6
	v_exp_f32_e32 v10, v10
	v_exp_f32_e32 v12, v14
	v_fma_f32 v4, v131, s12, s12
	v_fma_f32 v8, v130, s12, s12
	v_fma_f32 v14, v133, s12, s12
	v_fma_f32 v16, v132, s12, s12
	v_mfma_f32_32x32x16_bf16 v[18:33], v[114:117], v[166:169], v[18:33]
	v_exp_f32_e32 v3, v3
	v_fmac_f32_e32 v4, v2, v4
	v_exp_f32_e32 v2, v7
	v_fmac_f32_e32 v8, v6, v8
	v_exp_f32_e32 v6, v11
	v_exp_f32_e32 v7, v15
	v_fmac_f32_e32 v14, v10, v14
	v_fmac_f32_e32 v16, v12, v16
	v_mfma_f32_32x32x16_bf16 v[18:33], v[110:113], v[162:165], v[18:33]
	v_add_f32_e32 v10, 1.0, v3
	v_rcp_f32_e32 v3, v4
	v_add_f32_e32 v4, 1.0, v2
	v_rcp_f32_e32 v2, v8
	v_rcp_f32_e32 v135, v14
	v_rcp_f32_e32 v134, v16
	v_mfma_f32_32x32x16_bf16 v[18:33], v[106:109], v[174:177], v[18:33]
	v_add_f32_e32 v6, 1.0, v6
	v_add_f32_e32 v7, 1.0, v7
	v_rcp_f32_e32 v137, v10
	v_rcp_f32_e32 v136, v4
	v_exp_f32_e32 v140, v5
	v_exp_f32_e32 v141, v9
	v_mfma_f32_32x32x16_bf16 v[18:33], v[102:105], v[182:185], v[18:33]
	v_rcp_f32_e32 v139, v6
	v_rcp_f32_e32 v138, v7
	v_exp_f32_e32 v146, v13
	v_exp_f32_e32 v147, v17
	v_mfma_f32_32x32x16_bf16 v[18:33], v[98:101], v[142:145], v[18:33]
	v_fma_f32 v130, -v130, v2, v2
	v_fma_f32 v131, -v131, v3, v3
	v_pk_fma_f32 v[224:225], v[136:137], v[204:205], v[130:131]
	s_nop 0
	v_pk_fma_f32 v[130:131], v[132:133], v[134:135], v[134:135] neg_lo:[1,0,0] neg_hi:[1,0,0]
	s_nop 0
	v_pk_fma_f32 v[226:227], v[138:139], v[202:203], v[130:131]
	s_waitcnt lgkmcnt(0)
	v_mfma_f32_32x32x16_bf16 v[18:33], v[94:97], v[154:157], v[18:33]
	v_add_f32_e32 v130, 1.0, v140
	v_exp_f32_e32 v131, v225
	v_add_f32_e32 v132, 1.0, v141
	v_exp_f32_e32 v133, v224
	v_exp_f32_e32 v134, v227
	v_exp_f32_e32 v135, v226
	v_add_f32_e32 v136, 1.0, v146
	v_add_f32_e32 v137, 1.0, v147
	v_mfma_f32_32x32x16_bf16 v[18:33], v[90:93], v[158:161], v[18:33]
	v_fmac_f32_e32 v130, v130, v131
	v_fmac_f32_e32 v132, v132, v133
	v_fmac_f32_e32 v136, v136, v134
	v_fmac_f32_e32 v137, v137, v135
	v_mfma_f32_32x32x16_bf16 v[18:33], v[86:89], v[186:189], v[18:33]
	v_rcp_f32_e32 v130, v130
	v_rcp_f32_e32 v132, v132
	v_rcp_f32_e32 v136, v136
	v_rcp_f32_e32 v137, v137
	v_mfma_f32_32x32x16_bf16 v[18:33], v[82:85], v[190:193], v[18:33]
	v_fma_f32 v130, -v131, v130, v130
	v_fma_f32 v131, -v133, v132, v132
	v_fma_f32 v132, -v134, v136, v136
	v_fma_f32 v133, -v135, v137, v137
	v_cvt_pk_bf16_f32 v254, v130, v131
	v_cvt_pk_bf16_f32 v255, v132, v133
	ds_write_b128 v211, v[252:255] offset:0
	s_waitcnt lgkmcnt(0)
	s_barrier
	v_mfma_f32_32x32x16_bf16 v[2:17], v[78:81], v[194:197], v[236:251]
	ds_read_b128 v[202:205], v210
	v_add_u32_e32 v216, v230, v228
	v_mfma_f32_32x32x16_bf16 v[2:17], v[74:77], v[178:181], v[2:17]
	ds_read_b128 v[194:197], v210 offset:1024
	v_exp_f32_e32 v147, v20
	v_exp_f32_e32 v146, v24
	v_mfma_f32_32x32x16_bf16 v[2:17], v[70:73], v[170:173], v[2:17]
	ds_read_b128 v[138:141], v210 offset:2048
	v_exp_f32_e32 v149, v28
	v_exp_f32_e32 v148, v32
	v_exp_f32_e32 v18, v18
	v_exp_f32_e32 v22, v22
	v_exp_f32_e32 v24, v26
	v_exp_f32_e32 v26, v30
	v_fma_f32 v20, v147, s12, s12
	v_fma_f32 v28, v146, s12, s12
	v_fma_f32 v30, v149, s12, s12
	v_fma_f32 v32, v148, s12, s12
	v_mfma_f32_32x32x16_bf16 v[2:17], v[66:69], v[166:169], v[2:17]
	ds_read_b128 v[134:137], v210 offset:3072
	v_exp_f32_e32 v19, v19
	v_exp_f32_e32 v23, v23
	v_exp_f32_e32 v27, v27
	v_exp_f32_e32 v31, v31
	v_fmac_f32_e32 v20, v18, v20
	v_fmac_f32_e32 v28, v22, v28
	v_fmac_f32_e32 v30, v24, v30
	v_fmac_f32_e32 v32, v26, v32
	v_mfma_f32_32x32x16_bf16 v[2:17], v[62:65], v[162:165], v[2:17]
	ds_read_b128 v[166:169], v210 offset:4096
	v_add_f32_e32 v22, 1.0, v19
	v_rcp_f32_e32 v19, v20
	v_rcp_f32_e32 v18, v28
	v_rcp_f32_e32 v151, v30
	v_rcp_f32_e32 v150, v32
	v_add_f32_e32 v20, 1.0, v23
	v_mfma_f32_32x32x16_bf16 v[2:17], v[58:61], v[174:177], v[2:17]
	ds_read_b128 v[162:165], v210 offset:5120
	v_rcp_f32_e32 v153, v22
	v_rcp_f32_e32 v152, v20
	v_add_f32_e32 v23, 1.0, v27
	v_add_f32_e32 v20, 1.0, v31
	v_exp_f32_e32 v180, v21
	v_exp_f32_e32 v181, v25
	v_mfma_f32_32x32x16_bf16 v[2:17], v[54:57], v[182:185], v[2:17]
	ds_read_b128 v[170:173], v210 offset:6144
	v_rcp_f32_e32 v175, v23
	v_rcp_f32_e32 v174, v20
	v_exp_f32_e32 v176, v29
	v_exp_f32_e32 v177, v33
	v_mfma_f32_32x32x16_bf16 v[2:17], v[50:53], v[142:145], v[2:17]
	ds_read_b128 v[130:133], v210 offset:7168
	v_fma_f32 v146, -v146, v18, v18
	v_fma_f32 v147, -v147, v19, v19
	ds_read_b128 v[18:21], v231 offset:36928
	ds_read_b128 v[22:25], v231 offset:36944
	ds_read_b128 v[26:29], v231 offset:36960
	ds_read_b128 v[30:33], v231 offset:36976
	v_pk_fma_f32 v[220:221], v[152:153], v[200:201], v[146:147]
	v_pk_fma_f32 v[142:143], v[148:149], v[150:151], v[150:151] neg_lo:[1,0,0] neg_hi:[1,0,0]
	s_nop 0
	v_pk_fma_f32 v[222:223], v[174:175], v[198:199], v[142:143]
	v_mfma_f32_32x32x16_bf16 v[2:17], v[46:49], v[154:157], v[2:17]
	ds_read_b128 v[146:149], v216 offset:16384
	v_add_f32_e32 v142, 1.0, v180
	v_exp_f32_e32 v143, v221
	v_exp_f32_e32 v144, v220
	v_exp_f32_e32 v145, v223
	v_exp_f32_e32 v180, v222
	v_add_f32_e32 v154, 1.0, v181
	v_add_f32_e32 v155, 1.0, v176
	v_add_f32_e32 v156, 1.0, v177
	v_mfma_f32_32x32x16_bf16 v[2:17], v[42:45], v[158:161], v[2:17]
	ds_read_b128 v[150:153], v216 offset:16416
	v_fmac_f32_e32 v142, v142, v143
	v_fmac_f32_e32 v154, v154, v144
	v_fmac_f32_e32 v155, v155, v145
	v_fmac_f32_e32 v156, v156, v180
	v_mfma_f32_32x32x16_bf16 v[2:17], v[38:41], v[186:189], v[2:17]
	ds_read_b128 v[174:177], v216 offset:16448
	v_rcp_f32_e32 v142, v142
	v_rcp_f32_e32 v154, v154
	v_mfma_f32_32x32x16_bf16 v[2:17], v[34:37], v[190:193], v[2:17]
	ds_read_b128 v[198:201], v216 offset:16480
	v_rcp_f32_e32 v155, v155
	v_rcp_f32_e32 v156, v156
	v_fma_f32 v142, -v143, v142, v142
	v_fma_f32 v143, -v144, v154, v154
	s_waitcnt lgkmcnt(4)
	v_mfma_f32_32x32x16_bf16 v[18:33], v[126:129], v[202:205], v[18:33]
	v_fma_f32 v144, -v145, v155, v155
	v_fma_f32 v145, -v180, v156, v156
	v_cvt_pk_bf16_f32 v252, v142, v143
	v_cvt_pk_bf16_f32 v253, v144, v145
	v_mfma_f32_32x32x16_bf16 v[18:33], v[122:125], v[194:197], v[18:33]
	s_nop 1
	v_exp_f32_e32 v143, v4
	v_exp_f32_e32 v142, v8
	v_exp_f32_e32 v145, v12
	v_exp_f32_e32 v144, v16
	v_mfma_f32_32x32x16_bf16 v[18:33], v[118:121], v[138:141], v[18:33]
	v_exp_f32_e32 v2, v2
	v_exp_f32_e32 v6, v6
	v_exp_f32_e32 v10, v10
	v_exp_f32_e32 v12, v14
	v_fma_f32 v4, v143, s12, s12
	v_fma_f32 v8, v142, s12, s12
	v_fma_f32 v14, v145, s12, s12
	v_fma_f32 v16, v144, s12, s12
	v_mfma_f32_32x32x16_bf16 v[18:33], v[114:117], v[134:137], v[18:33]
	v_exp_f32_e32 v3, v3
	v_fmac_f32_e32 v4, v2, v4
	v_exp_f32_e32 v2, v7
	v_fmac_f32_e32 v8, v6, v8
	v_exp_f32_e32 v6, v11
	v_exp_f32_e32 v7, v15
	v_fmac_f32_e32 v14, v10, v14
	v_fmac_f32_e32 v16, v12, v16
	v_mfma_f32_32x32x16_bf16 v[18:33], v[110:113], v[166:169], v[18:33]
	v_add_f32_e32 v10, 1.0, v3
	v_rcp_f32_e32 v3, v4
	v_add_f32_e32 v4, 1.0, v2
	v_rcp_f32_e32 v2, v8
	v_rcp_f32_e32 v155, v14
	v_rcp_f32_e32 v154, v16
	v_mfma_f32_32x32x16_bf16 v[18:33], v[106:109], v[162:165], v[18:33]
	v_add_f32_e32 v6, 1.0, v6
	v_add_f32_e32 v7, 1.0, v7
	v_rcp_f32_e32 v157, v10
	v_rcp_f32_e32 v156, v4
	v_exp_f32_e32 v160, v5
	v_exp_f32_e32 v161, v9
	v_mfma_f32_32x32x16_bf16 v[18:33], v[102:105], v[170:173], v[18:33]
	v_rcp_f32_e32 v159, v6
	v_rcp_f32_e32 v158, v7
	v_exp_f32_e32 v180, v13
	v_exp_f32_e32 v181, v17
	v_mfma_f32_32x32x16_bf16 v[18:33], v[98:101], v[130:133], v[18:33]
	v_fma_f32 v142, -v142, v2, v2
	v_fma_f32 v143, -v143, v3, v3
	v_pk_fma_f32 v[216:217], v[156:157], v[206:207], v[142:143]
	s_nop 0
	v_pk_fma_f32 v[142:143], v[144:145], v[154:155], v[154:155] neg_lo:[1,0,0] neg_hi:[1,0,0]
	s_nop 0
	v_pk_fma_f32 v[218:219], v[158:159], v[208:209], v[142:143]
	s_waitcnt lgkmcnt(0)
	v_mfma_f32_32x32x16_bf16 v[18:33], v[94:97], v[146:149], v[18:33]
	v_add_f32_e32 v142, 1.0, v160
	v_exp_f32_e32 v143, v217
	v_add_f32_e32 v144, 1.0, v161
	v_exp_f32_e32 v145, v216
	v_exp_f32_e32 v154, v219
	v_exp_f32_e32 v155, v218
	v_add_f32_e32 v156, 1.0, v180
	v_add_f32_e32 v157, 1.0, v181
	v_mfma_f32_32x32x16_bf16 v[18:33], v[90:93], v[150:153], v[18:33]
	v_fmac_f32_e32 v142, v142, v143
	v_fmac_f32_e32 v144, v144, v145
	v_fmac_f32_e32 v156, v156, v154
	v_fmac_f32_e32 v157, v157, v155
	v_mfma_f32_32x32x16_bf16 v[18:33], v[86:89], v[174:177], v[18:33]
	v_rcp_f32_e32 v142, v142
	v_rcp_f32_e32 v144, v144
	v_rcp_f32_e32 v156, v156
	v_rcp_f32_e32 v157, v157
	v_mfma_f32_32x32x16_bf16 v[18:33], v[82:85], v[198:201], v[18:33]
	v_fma_f32 v142, -v143, v142, v142
	v_fma_f32 v143, -v145, v144, v144
	v_fma_f32 v144, -v154, v156, v156
	v_fma_f32 v145, -v155, v157, v157
	v_cvt_pk_bf16_f32 v254, v142, v143
	v_cvt_pk_bf16_f32 v255, v144, v145
	ds_write_b128 v211, v[252:255] offset:8192
	s_waitcnt lgkmcnt(0)
	s_barrier
	v_mfma_f32_32x32x16_bf16 v[2:17], v[78:81], v[202:205], v[236:251]
	v_add_u32_e32 v234, v230, v229
	ds_read2_b32 v[228:229], v232 offset0:64 offset1:96
	ds_read_b128 v[206:209], v210 offset:8192
	v_mfma_f32_32x32x16_bf16 v[2:17], v[74:77], v[194:197], v[2:17]
	ds_read_b128 v[190:193], v210 offset:9216
	v_exp_f32_e32 v179, v20
	v_exp_f32_e32 v178, v24
	v_mfma_f32_32x32x16_bf16 v[2:17], v[70:73], v[138:141], v[2:17]
	ds_read_b128 v[158:161], v210 offset:10240
	v_exp_f32_e32 v181, v28
	v_exp_f32_e32 v180, v32
	v_exp_f32_e32 v18, v18
	v_exp_f32_e32 v22, v22
	v_exp_f32_e32 v24, v26
	v_exp_f32_e32 v26, v30
	v_fma_f32 v20, v179, s12, s12
	v_fma_f32 v28, v178, s12, s12
	v_fma_f32 v30, v181, s12, s12
	v_fma_f32 v32, v180, s12, s12
	v_mfma_f32_32x32x16_bf16 v[2:17], v[66:69], v[134:137], v[2:17]
	ds_read_b128 v[142:145], v210 offset:11264
	v_exp_f32_e32 v19, v19
	v_exp_f32_e32 v23, v23
	v_exp_f32_e32 v27, v27
	v_exp_f32_e32 v31, v31
	v_fmac_f32_e32 v20, v18, v20
	v_fmac_f32_e32 v28, v22, v28
	v_fmac_f32_e32 v30, v24, v30
	v_fmac_f32_e32 v32, v26, v32
	v_mfma_f32_32x32x16_bf16 v[2:17], v[62:65], v[166:169], v[2:17]
	ds_read_b128 v[154:157], v210 offset:12288
	v_add_f32_e32 v22, 1.0, v19
	v_rcp_f32_e32 v19, v20
	v_rcp_f32_e32 v18, v28
	v_rcp_f32_e32 v139, v30
	v_rcp_f32_e32 v138, v32
	v_add_f32_e32 v20, 1.0, v23
	v_mfma_f32_32x32x16_bf16 v[2:17], v[58:61], v[162:165], v[2:17]
	ds_read_b128 v[182:185], v210 offset:13312
	v_rcp_f32_e32 v141, v22
	v_rcp_f32_e32 v140, v20
	v_add_f32_e32 v23, 1.0, v27
	v_add_f32_e32 v20, 1.0, v31
	v_exp_f32_e32 v168, v21
	v_exp_f32_e32 v169, v25
	v_mfma_f32_32x32x16_bf16 v[2:17], v[54:57], v[170:173], v[2:17]
	ds_read_b128 v[186:189], v210 offset:14336
	v_rcp_f32_e32 v163, v23
	v_rcp_f32_e32 v162, v20
	v_exp_f32_e32 v194, v29
	v_exp_f32_e32 v195, v33
	v_mfma_f32_32x32x16_bf16 v[2:17], v[50:53], v[130:133], v[2:17]
	ds_read_b128 v[134:137], v210 offset:15360
	v_fma_f32 v166, -v178, v18, v18
	v_fma_f32 v167, -v179, v19, v19
	ds_read_b128 v[18:21], v231 offset:36928
	ds_read_b128 v[22:25], v231 offset:36944
	ds_read_b128 v[26:29], v231 offset:36960
	ds_read_b128 v[30:33], v231 offset:36976
	v_pk_fma_f32 v[214:215], v[140:141], v[214:215], v[166:167]
	v_pk_fma_f32 v[130:131], v[180:181], v[138:139], v[138:139] neg_lo:[1,0,0] neg_hi:[1,0,0]
	s_nop 0
	v_pk_fma_f32 v[212:213], v[162:163], v[212:213], v[130:131]
	v_mfma_f32_32x32x16_bf16 v[2:17], v[46:49], v[146:149], v[2:17]
	ds_read_b128 v[138:141], v234 offset:16384
	v_add_f32_e32 v130, 1.0, v168
	v_exp_f32_e32 v131, v215
	v_exp_f32_e32 v132, v214
	v_exp_f32_e32 v133, v213
	v_exp_f32_e32 v162, v212
	v_add_f32_e32 v163, 1.0, v169
	v_add_f32_e32 v166, 1.0, v194
	v_add_f32_e32 v167, 1.0, v195
	v_mfma_f32_32x32x16_bf16 v[2:17], v[42:45], v[150:153], v[2:17]
	ds_read_b128 v[146:149], v234 offset:16416
	v_fmac_f32_e32 v130, v130, v131
	v_fmac_f32_e32 v163, v163, v132
	v_fmac_f32_e32 v166, v166, v133
	v_fmac_f32_e32 v167, v167, v162
	v_mfma_f32_32x32x16_bf16 v[2:17], v[38:41], v[174:177], v[2:17]
	ds_read_b128 v[150:153], v234 offset:16448
	v_rcp_f32_e32 v130, v130
	v_rcp_f32_e32 v163, v163
	v_mfma_f32_32x32x16_bf16 v[2:17], v[34:37], v[198:201], v[2:17]
	ds_read_b128 v[178:181], v234 offset:16480
	v_rcp_f32_e32 v166, v166
	v_rcp_f32_e32 v167, v167
	v_fma_f32 v130, -v131, v130, v130
	v_fma_f32 v131, -v132, v163, v163
	s_waitcnt lgkmcnt(4)
	v_mfma_f32_32x32x16_bf16 v[18:33], v[126:129], v[206:209], v[18:33]
	v_fma_f32 v132, -v133, v166, v166
	v_fma_f32 v133, -v162, v167, v167
	v_cvt_pk_bf16_f32 v252, v130, v131
	v_cvt_pk_bf16_f32 v253, v132, v133
	v_mfma_f32_32x32x16_bf16 v[18:33], v[122:125], v[190:193], v[18:33]
	s_nop 1
	v_exp_f32_e32 v131, v4
	v_exp_f32_e32 v130, v8
	v_exp_f32_e32 v133, v12
	v_exp_f32_e32 v132, v16
	v_mfma_f32_32x32x16_bf16 v[18:33], v[118:121], v[158:161], v[18:33]
	v_exp_f32_e32 v2, v2
	v_exp_f32_e32 v6, v6
	v_exp_f32_e32 v10, v10
	v_exp_f32_e32 v12, v14
	v_fma_f32 v4, v131, s12, s12
	v_fma_f32 v8, v130, s12, s12
	v_fma_f32 v14, v133, s12, s12
	v_fma_f32 v16, v132, s12, s12
	v_mfma_f32_32x32x16_bf16 v[18:33], v[114:117], v[142:145], v[18:33]
	v_exp_f32_e32 v3, v3
	v_fmac_f32_e32 v4, v2, v4
	v_exp_f32_e32 v2, v7
	v_fmac_f32_e32 v8, v6, v8
	v_exp_f32_e32 v6, v11
	v_exp_f32_e32 v7, v15
	v_fmac_f32_e32 v14, v10, v14
	v_fmac_f32_e32 v16, v12, v16
	v_mfma_f32_32x32x16_bf16 v[18:33], v[110:113], v[154:157], v[18:33]
	v_add_f32_e32 v10, 1.0, v3
	v_rcp_f32_e32 v3, v4
	v_add_f32_e32 v4, 1.0, v2
	v_rcp_f32_e32 v2, v8
	v_rcp_f32_e32 v163, v14
	v_rcp_f32_e32 v162, v16
	v_mfma_f32_32x32x16_bf16 v[18:33], v[106:109], v[182:185], v[18:33]
	v_add_f32_e32 v6, 1.0, v6
	v_add_f32_e32 v7, 1.0, v7
	v_rcp_f32_e32 v167, v10
	v_rcp_f32_e32 v166, v4
	v_exp_f32_e32 v170, v5
	v_exp_f32_e32 v171, v9
	v_mfma_f32_32x32x16_bf16 v[18:33], v[102:105], v[186:189], v[18:33]
	v_rcp_f32_e32 v169, v6
	v_rcp_f32_e32 v168, v7
	v_exp_f32_e32 v172, v13
	v_exp_f32_e32 v173, v17
	v_mfma_f32_32x32x16_bf16 v[18:33], v[98:101], v[134:137], v[18:33]
	v_fma_f32 v130, -v130, v2, v2
	v_fma_f32 v131, -v131, v3, v3
	v_pk_fma_f32 v[204:205], v[166:167], v[224:225], v[130:131]
	s_nop 0
	v_pk_fma_f32 v[130:131], v[132:133], v[162:163], v[162:163] neg_lo:[1,0,0] neg_hi:[1,0,0]
	s_nop 0
	v_pk_fma_f32 v[202:203], v[168:169], v[226:227], v[130:131]
	s_waitcnt lgkmcnt(0)
	v_mfma_f32_32x32x16_bf16 v[18:33], v[94:97], v[138:141], v[18:33]
	v_add_f32_e32 v130, 1.0, v170
	v_exp_f32_e32 v131, v205
	v_add_f32_e32 v132, 1.0, v171
	v_exp_f32_e32 v133, v204
	v_exp_f32_e32 v162, v203
	v_exp_f32_e32 v163, v202
	v_add_f32_e32 v164, 1.0, v172
	v_add_f32_e32 v165, 1.0, v173
	v_mfma_f32_32x32x16_bf16 v[18:33], v[90:93], v[146:149], v[18:33]
	v_fmac_f32_e32 v130, v130, v131
	v_fmac_f32_e32 v132, v132, v133
	v_fmac_f32_e32 v164, v164, v162
	v_fmac_f32_e32 v165, v165, v163
	v_mfma_f32_32x32x16_bf16 v[18:33], v[86:89], v[150:153], v[18:33]
	v_rcp_f32_e32 v130, v130
	v_rcp_f32_e32 v132, v132
	v_rcp_f32_e32 v164, v164
	v_rcp_f32_e32 v165, v165
	v_mfma_f32_32x32x16_bf16 v[18:33], v[82:85], v[178:181], v[18:33]
	v_fma_f32 v130, -v131, v130, v130
	v_fma_f32 v131, -v133, v132, v132
	v_fma_f32 v132, -v162, v164, v164
	v_fma_f32 v133, -v163, v165, v165
	v_cvt_pk_bf16_f32 v254, v130, v131
	v_cvt_pk_bf16_f32 v255, v132, v133
	ds_write_b128 v211, v[252:255] offset:0
	s_waitcnt lgkmcnt(0)
	s_barrier
	s_branch .LBB1_13
